# nt hint also on the scan A stores (RWKV chunk records written once, read once by the chains)
# speedup vs baseline: 1.0657x; 1.0006x over previous
.LBB0_310:
	s_or_b64 exec, exec, s[0:1]
	s_waitcnt lgkmcnt(0)
	s_barrier
	ds_read_b128 v[26:29], v110 offset:27904
	ds_read_b128 v[30:33], v109 offset:42240
	s_mov_b64 s[0:1], 0x3c00
	s_mov_b32 s37, s22
	s_waitcnt lgkmcnt(0)
	v_mfma_f32_16x16x32_bf16 v[30:33], v[26:29], v[30:33], 0
	s_nop 7
	v_cvt_pk_bf16_f32 v30, v30, v31
	v_cvt_pk_bf16_f32 v31, v32, v33
	v_lshl_add_u64 v[32:33], v[54:55], 0, v[48:49]
	v_lshl_add_u64 v[54:55], v[32:33], 0, s[0:1]
	s_movk_i32 s0, 0x3000
	v_add_co_u32_e32 v32, vcc, s0, v32
	s_nop 1
	v_addc_co_u32_e32 v33, vcc, 0, v33, vcc
	global_store_dwordx2 v[32:33], v[30:31], off offset:3072 nt
	ds_read_b128 v[30:33], v109 offset:43520
	s_waitcnt lgkmcnt(0)
	v_mfma_f32_16x16x32_bf16 v[30:33], v[26:29], v[30:33], 0
	s_and_b64 vcc, exec, s[8:9]
	s_nop 6
	v_cvt_pk_bf16_f32 v30, v30, v31
	v_cvt_pk_bf16_f32 v31, v32, v33
	global_store_dwordx2 v[54:55], v[30:31], off offset:512 nt
	ds_read_b128 v[30:33], v109 offset:44800
	s_waitcnt lgkmcnt(0)
	v_mfma_f32_16x16x32_bf16 v[30:33], v[26:29], v[30:33], 0
	s_nop 7
	v_cvt_pk_bf16_f32 v30, v30, v31
	v_cvt_pk_bf16_f32 v31, v32, v33
	global_store_dwordx2 v[54:55], v[30:31], off offset:1024 nt
	ds_read_b128 v[30:33], v109 offset:46080
	s_waitcnt lgkmcnt(0)
	v_mfma_f32_16x16x32_bf16 v[26:29], v[26:29], v[30:33], 0
	s_nop 7
	v_cvt_pk_bf16_f32 v26, v26, v27
	v_cvt_pk_bf16_f32 v27, v28, v29
	global_store_dwordx2 v[54:55], v[26:27], off offset:1536 nt
	s_waitcnt lgkmcnt(0)
	s_barrier
	s_waitcnt vmcnt(4)
	v_lshlrev_b32_e32 v6, 16, v12
	v_lshlrev_b32_e32 v2, 16, v4
	v_and_b32_e32 v3, 0xffff0000, v4
	v_lshlrev_b32_e32 v4, 16, v5
	v_and_b32_e32 v5, 0xffff0000, v5
	v_and_b32_e32 v7, 0xffff0000, v12
	v_lshlrev_b32_e32 v8, 16, v13
	v_and_b32_e32 v9, 0xffff0000, v13
	v_lshlrev_b32_e32 v10, 16, v14
	v_and_b32_e32 v11, 0xffff0000, v14
	v_lshlrev_b32_e32 v12, 16, v15
	v_and_b32_e32 v13, 0xffff0000, v15
	v_lshlrev_b32_e32 v14, 16, v16
	v_and_b32_e32 v15, 0xffff0000, v16
	v_lshlrev_b32_e32 v16, 16, v17
	v_and_b32_e32 v17, 0xffff0000, v17
	v_lshlrev_b32_e32 v18, 16, v20
	v_and_b32_e32 v19, 0xffff0000, v20
	v_lshlrev_b32_e32 v20, 16, v21
	v_and_b32_e32 v21, 0xffff0000, v21
	v_lshlrev_b32_e32 v22, 16, v24
	v_and_b32_e32 v23, 0xffff0000, v24
	v_lshlrev_b32_e32 v24, 16, v25
	v_and_b32_e32 v25, 0xffff0000, v25
	s_cbranch_vccnz .LBB0_392

.LBB0_349:
	s_or_b64 exec, exec, s[0:1]
	v_mov_b32_e32 v37, 0
	v_mov_b32_e32 v56, 0
	s_and_saveexec_b64 s[0:1], s[76:77]
	ds_read_b32 v56, v105 offset:27648
	s_or_b64 exec, exec, s[0:1]
	v_lshl_add_u32 v57, s37, 1, v39
	s_mov_b32 s0, 0x78787879
	v_mul_hi_i32 v58, v57, s0
	v_lshrrev_b32_e32 v59, 31, v58
	v_ashrrev_i32_e32 v58, 7, v58
	v_add_u32_e32 v58, v58, v59
	s_waitcnt lgkmcnt(0)
	v_sub_f32_e32 v131, v54, v30
	v_mul_i32_i24_e32 v30, 0x110, v58
	v_sub_u32_e32 v54, v57, v30
	v_sub_f32_e32 v132, v55, v31
	v_mul_hi_i32_i24_e32 v31, 0x110, v58
	v_ashrrev_i32_e32 v55, 31, v54
	v_lshl_add_u64 v[58:59], v[30:31], 0, v[54:55]
	s_movk_i32 s0, 0x5c00
	v_mov_b64_e32 v[30:31], s[30:31]
	v_sub_f32_e32 v32, v34, v32
	v_mul_lo_u32 v34, v59, s0
	v_mad_u64_u32 v[54:55], s[0:1], v58, s0, v[30:31]
	v_add_u32_e32 v55, v34, v55
	v_sub_f32_e32 v30, v56, v33
	v_cvt_pk_bf16_f32 v31, v32, v30
	v_cvt_pk_bf16_f32 v30, v131, v132
	v_lshl_add_u64 v[56:57], v[54:55], 0, v[44:45]
	global_store_dwordx2 v[56:57], v[30:31], off nt
	ds_read_b128 v[30:33], v109 offset:48640
	s_waitcnt lgkmcnt(0)
	v_mfma_f32_16x16x32_bf16 v[30:33], v[30:33], v[26:29], 0
	s_movk_i32 s14, 0x5c00
	s_and_saveexec_b64 s[0:1], s[78:79]
	ds_read_b32 v37, v105 offset:27648
	s_or_b64 exec, exec, s[0:1]
	v_mov_b32_e32 v131, 0
	v_mov_b32_e32 v132, 0
	s_and_saveexec_b64 s[0:1], s[80:81]
	ds_read_b32 v132, v105 offset:27648
	s_or_b64 exec, exec, s[0:1]
	s_and_saveexec_b64 s[0:1], s[82:83]
	ds_read_b32 v131, v105 offset:27648
	s_or_b64 exec, exec, s[0:1]
	v_mov_b32_e32 v59, 0
	v_mov_b32_e32 v133, 0
	s_and_saveexec_b64 s[0:1], s[84:85]
	ds_read_b32 v133, v105 offset:27648
	s_or_b64 exec, exec, s[0:1]
	s_waitcnt lgkmcnt(0)
	v_sub_f32_e32 v30, v37, v30
	v_sub_f32_e32 v37, v132, v31
	v_sub_f32_e32 v31, v131, v32
	v_sub_f32_e32 v32, v133, v33
	v_cvt_pk_bf16_f32 v31, v31, v32
	v_cvt_pk_bf16_f32 v30, v30, v37
	global_store_dwordx2 v[56:57], v[30:31], off offset:8 nt
	ds_read_b128 v[30:33], v109 offset:49920
	s_waitcnt lgkmcnt(0)
	v_mfma_f32_16x16x32_bf16 v[30:33], v[30:33], v[26:29], 0
	s_and_saveexec_b64 s[0:1], s[86:87]
	ds_read_b32 v59, v105 offset:27648
	s_or_b64 exec, exec, s[0:1]
	v_mov_b32_e32 v131, 0
	v_mov_b32_e32 v132, 0
	s_and_saveexec_b64 s[0:1], s[88:89]
	ds_read_b32 v132, v105 offset:27648
	s_or_b64 exec, exec, s[0:1]
	s_and_saveexec_b64 s[0:1], s[90:91]
	ds_read_b32 v131, v105 offset:27648
	s_or_b64 exec, exec, s[0:1]
	v_mov_b32_e32 v37, 0
	v_mov_b32_e32 v133, 0
	s_and_saveexec_b64 s[0:1], s[92:93]
	ds_read_b32 v133, v105 offset:27648
	s_or_b64 exec, exec, s[0:1]
	s_waitcnt lgkmcnt(0)
	v_sub_f32_e32 v30, v59, v30
	v_sub_f32_e32 v59, v132, v31
	v_sub_f32_e32 v31, v131, v32
	v_sub_f32_e32 v32, v133, v33
	v_cvt_pk_bf16_f32 v31, v31, v32
	v_cvt_pk_bf16_f32 v30, v30, v59
	global_store_dwordx2 v[56:57], v[30:31], off offset:1024 nt
	ds_read_b128 v[30:33], v109 offset:51200
	s_waitcnt lgkmcnt(0)
	v_mfma_f32_16x16x32_bf16 v[26:29], v[30:33], v[26:29], 0
	s_and_saveexec_b64 s[0:1], s[94:95]
	ds_read_b32 v37, v105 offset:27648
	s_or_b64 exec, exec, s[0:1]
	v_mov_b32_e32 v32, 0
	v_mov_b32_e32 v33, 0
	s_and_saveexec_b64 s[0:1], s[96:97]
	s_cbranch_execnz .LBB0_385
	s_or_b64 exec, exec, s[0:1]
	s_and_saveexec_b64 s[0:1], s[2:3]
	s_cbranch_execnz .LBB0_386

.LBB0_373:
	s_or_b64 exec, exec, s[0:1]
	v_mad_u64_u32 v[30:31], s[0:1], v58, s14, 0
	v_add_u32_e32 v31, v31, v34
	s_waitcnt lgkmcnt(0)
	v_sub_f32_e32 v34, v37, v26
	v_sub_f32_e32 v33, v33, v27
	v_sub_f32_e32 v28, v32, v28
	v_sub_f32_e32 v29, v59, v29
	v_cvt_pk_bf16_f32 v29, v28, v29
	v_cvt_pk_bf16_f32 v28, v34, v33
	global_store_dwordx2 v[56:57], v[28:29], off offset:1032 nt
	ds_read_b128 v[56:59], v110 offset:47360
	ds_read_b128 v[132:135], v109 offset:53760
	s_waitcnt lgkmcnt(0)
	v_mfma_f32_16x16x32_bf16 v[56:59], v[56:59], v[132:135], 0
	ds_read_b128 v[132:135], v126
	v_lshl_add_u64 v[26:27], v[54:55], 0, v[42:43]
	s_mov_b64 s[0:1], 0x2800
	v_lshl_add_u64 v[26:27], v[26:27], 0, s[0:1]
	s_mov_b32 s6, s36
	s_waitcnt lgkmcnt(0)
	s_nop 1
	v_sub_f32_e32 v28, v132, v56
	v_sub_f32_e32 v29, v134, v58
	v_sub_f32_e32 v32, v133, v57
	v_cvt_pk_bf16_f32 v28, v28, s0
	v_cvt_pk_bf16_f32 v29, v32, v29
	s_mov_b32 s0, 0x5040100
	v_sub_f32_e32 v32, v135, v59
	v_cvt_pk_bf16_f32 v32, v32, s0
	v_perm_b32 v28, v29, v28, s0
	v_alignbit_b32 v29, v32, v29, 16
	v_lshl_add_u64 v[32:33], v[54:55], 0, v[46:47]
	v_add_co_u32_e32 v32, vcc, 0x2000, v32
	s_nop 1
	v_addc_co_u32_e32 v33, vcc, 0, v33, vcc
	global_store_dwordx2 v[32:33], v[28:29], off nt
	v_mov_b32_e32 v28, v119
	v_mov_b32_e32 v29, v106
	v_mov_b32_e32 v32, v118
	s_branch .LBB0_375

.LBB0_377:
	s_andn2_b64 vcc, exec, s[0:1]
	s_cbranch_vccnz .LBB0_374
	ds_read_b128 v[56:59], v109 offset:52480
	ds_read_b128 v[132:135], v109 offset:53760
	v_add_u32_e32 v33, v70, v73
	v_add_u32_e32 v33, 0x6400, v33
	s_waitcnt lgkmcnt(0)
	v_mfma_f32_16x16x32_bf16 v[56:59], v[56:59], v[132:135], 0
	ds_read2_b32 v[132:133], v33 offset1:16
	ds_read2_b32 v[134:135], v33 offset0:32 offset1:48
	s_waitcnt lgkmcnt(0)
	s_nop 4
	v_sub_f32_e32 v34, v132, v56
	v_mov_b32_e32 v132, v133
	v_mov_b32_e32 v133, v134
	v_mov_b32_e32 v56, v57
	v_mov_b32_e32 v57, v58
	v_pk_add_f32 v[56:57], v[132:133], v[56:57] neg_lo:[0,1] neg_hi:[0,1]
	v_cvt_pk_bf16_f32 v34, v34, s0
	v_cvt_pk_bf16_f32 v33, v56, v57
	s_mov_b32 s0, 0x5040100
	v_perm_b32 v56, v33, v34, s0
	v_sub_f32_e32 v34, v135, v59
	v_cvt_pk_bf16_f32 v34, v34, s0
	v_alignbit_b32 v57, v34, v33, 16
	global_store_dwordx2 v[26:27], v[56:57], off nt
	global_store_dwordx2 v[26:27], v[166:167], off offset:512 nt
	s_branch .LBB0_374

.LBB0_380:
	s_or_b64 exec, exec, s[6:7]
	v_add_u32_e32 v29, 0x100, v29
	s_movk_i32 s6, 0x2ff
	v_cmp_lt_u32_e32 vcc, s6, v29
	s_mov_b64 s[6:7], 0x400
	global_store_dword v[26:27], v30, off nt
	v_add_u32_e32 v28, 64, v28
	s_or_b64 s[0:1], vcc, s[0:1]
	v_lshl_add_u64 v[26:27], v[26:27], 0, s[6:7]
	s_andn2_b64 exec, exec, s[0:1]
	s_cbranch_execz .LBB0_310

.LBB0_474:
	v_mul_f32_e32 v3, 0x3fb8aa3b, v4
	v_exp_f32_e32 v3, v3
	s_waitcnt lgkmcnt(1)
	v_and_b32_e32 v2, 0xffff0000, v7
	s_lshl_b32 s0, s15, 3
	s_add_i32 s0, s19, s0
	v_mul_f32_e32 v2, v3, v2
	s_mov_b32 s2, 0
	v_cvt_pk_bf16_f32 v2, v2, s0
	s_mov_b32 s3, 1
	s_mov_b32 s69, s2
	ds_write_b16 v90, v2 offset:5376
	v_lshl_add_u64 v[2:3], v[10:11], 0, s[68:69]
	v_mov_b32_e32 v29, v35
	v_lshl_add_u64 v[14:15], v[2:3], 0, v[28:29]
	global_load_dwordx4 v[2:5], v[14:15], off offset:560
	global_load_dwordx4 v[6:9], v[14:15], off offset:544
	global_load_dwordx4 v[10:13], v[14:15], off offset:528
	s_nop 0
	global_load_dwordx4 v[14:17], v[14:15], off offset:512
	s_mul_hi_i32 s8, s0, 0x88
	s_mul_i32 s9, s0, 0x88
	s_waitcnt vmcnt(0)
	v_lshlrev_b32_e32 v27, 16, v14
	v_and_b32_e32 v14, 0xffff0000, v14
	v_lshlrev_b32_e32 v29, 16, v15
	v_cvt_pk_bf16_f32 v14, v14, s0
	v_and_b32_e32 v15, 0xffff0000, v15
	ds_write_b16 v88, v14 offset:6896
	v_cvt_pk_bf16_f32 v14, v29, s0
	ds_write_b16 v88, v14 offset:6976
	v_cvt_pk_bf16_f32 v14, v15, s0
	ds_write_b16 v88, v14 offset:7056
	v_lshlrev_b32_e32 v14, 16, v16
	v_and_b32_e32 v15, 0xffff0000, v16
	v_cvt_pk_bf16_f32 v14, v14, s0
	v_lshlrev_b32_e32 v16, 16, v17
	ds_write_b16 v88, v14 offset:7136
	v_cvt_pk_bf16_f32 v14, v15, s0
	v_and_b32_e32 v17, 0xffff0000, v17
	ds_write_b16 v88, v14 offset:7216
	v_cvt_pk_bf16_f32 v14, v16, s0
	ds_write_b16 v88, v14 offset:7296
	v_cvt_pk_bf16_f32 v14, v17, s0
	ds_write_b16 v88, v14 offset:7376
	v_lshlrev_b32_e32 v14, 16, v10
	v_and_b32_e32 v10, 0xffff0000, v10
	v_lshlrev_b32_e32 v15, 16, v11
	v_cvt_pk_bf16_f32 v10, v10, s0
	v_and_b32_e32 v11, 0xffff0000, v11
	ds_write_b16 v88, v10 offset:7536
	v_cvt_pk_bf16_f32 v10, v15, s0
	ds_write_b16 v88, v10 offset:7616
	v_cvt_pk_bf16_f32 v10, v11, s0
	ds_write_b16 v88, v10 offset:7696
	v_lshlrev_b32_e32 v10, 16, v12
	v_and_b32_e32 v11, 0xffff0000, v12
	v_cvt_pk_bf16_f32 v10, v10, s0
	v_lshlrev_b32_e32 v12, 16, v13
	ds_write_b16 v88, v10 offset:7776
	v_cvt_pk_bf16_f32 v10, v11, s0
	v_and_b32_e32 v13, 0xffff0000, v13
	ds_write_b16 v88, v10 offset:7856
	v_cvt_pk_bf16_f32 v10, v12, s0
	ds_write_b16 v88, v10 offset:7936
	v_cvt_pk_bf16_f32 v10, v13, s0
	ds_write_b16 v88, v10 offset:8016
	v_lshlrev_b32_e32 v10, 16, v6
	v_and_b32_e32 v6, 0xffff0000, v6
	v_lshlrev_b32_e32 v11, 16, v7
	v_cvt_pk_bf16_f32 v6, v6, s0
	v_and_b32_e32 v7, 0xffff0000, v7
	ds_write_b16 v88, v6 offset:8176
	v_cvt_pk_bf16_f32 v6, v11, s0
	ds_write_b16 v88, v6 offset:8256
	v_cvt_pk_bf16_f32 v6, v7, s0
	ds_write_b16 v88, v6 offset:8336
	v_lshlrev_b32_e32 v6, 16, v8
	v_and_b32_e32 v7, 0xffff0000, v8
	v_cvt_pk_bf16_f32 v6, v6, s0
	v_lshlrev_b32_e32 v8, 16, v9
	ds_write_b16 v88, v6 offset:8416
	v_cvt_pk_bf16_f32 v6, v7, s0
	v_and_b32_e32 v9, 0xffff0000, v9
	ds_write_b16 v88, v6 offset:8496
	v_cvt_pk_bf16_f32 v6, v8, s0
	ds_write_b16 v88, v6 offset:8576
	v_cvt_pk_bf16_f32 v6, v9, s0
	ds_write_b16 v88, v6 offset:8656
	v_lshlrev_b32_e32 v6, 16, v2
	v_and_b32_e32 v2, 0xffff0000, v2
	v_lshlrev_b32_e32 v7, 16, v3
	v_cvt_pk_bf16_f32 v2, v2, s0
	v_and_b32_e32 v3, 0xffff0000, v3
	ds_write_b16 v88, v2 offset:8816
	v_cvt_pk_bf16_f32 v2, v7, s0
	ds_write_b16 v88, v2 offset:8896
	v_cvt_pk_bf16_f32 v2, v3, s0
	ds_write_b16 v88, v2 offset:8976
	v_lshlrev_b32_e32 v2, 16, v4
	v_and_b32_e32 v3, 0xffff0000, v4
	v_cvt_pk_bf16_f32 v2, v2, s0
	v_lshlrev_b32_e32 v4, 16, v5
	ds_write_b16 v88, v2 offset:9056
	v_cvt_pk_bf16_f32 v2, v3, s0
	v_and_b32_e32 v5, 0xffff0000, v5
	ds_write_b16 v88, v2 offset:9136
	v_cvt_pk_bf16_f32 v2, v4, s0
	v_cvt_pk_bf16_f32 v27, v27, s0
	v_cvt_pk_bf16_f32 v14, v14, s0
	v_cvt_pk_bf16_f32 v10, v10, s0
	v_cvt_pk_bf16_f32 v6, v6, s0
	ds_write_b16 v88, v2 offset:9216
	v_cvt_pk_bf16_f32 v2, v5, s0
	ds_write_b16 v88, v27 offset:6816
	ds_write_b16 v88, v14 offset:7456
	ds_write_b16 v88, v10 offset:8096
	ds_write_b16 v88, v6 offset:8736
	ds_write_b16 v89, v2 offset:6816
	s_and_saveexec_b64 s[0:1], s[40:41]
	s_xor_b64 s[0:1], exec, s[0:1]
	s_add_u32 s2, s9, s14
	s_addc_u32 s3, s8, 0
	s_or_saveexec_b64 s[0:1], s[0:1]
	v_mov_b64_e32 v[2:3], s[2:3]
	s_xor_b64 exec, exec, s[0:1]
	s_cbranch_execz .LBB0_478
	ds_read_b32 v2, v80 offset:4092
	s_add_u32 s2, s9, s14
	s_addc_u32 s3, s8, 0
	s_lshl_b64 s[8:9], s[2:3], 7
	s_waitcnt lgkmcnt(0)
	v_mul_f32_e32 v2, 0x3fb8aa3b, v2
	v_exp_f32_e32 v4, v2
	v_lshl_add_u64 v[2:3], v[22:23], 0, s[8:9]
	global_store_dword v[2:3], v4, off nt
	v_mov_b64_e32 v[2:3], s[2:3]
.LBB0_478:
	s_or_b64 exec, exec, s[0:1]
	s_waitcnt lgkmcnt(0)
	v_lshlrev_b64 v[2:3], 13, v[2:3]
	v_lshl_add_u64 v[10:11], s[58:59], 0, v[2:3]
	ds_read_b128 v[12:15], v81 offset:6816
	ds_read_b128 v[2:5], v81 offset:4256
	v_mov_b32_e32 v31, v35
	v_lshl_add_u64 v[16:17], v[10:11], 0, v[30:31]
	s_waitcnt lgkmcnt(0)
	v_mfma_f32_16x16x32_bf16 v[6:9], v[12:15], v[2:5], 0
	v_mov_b32_e32 v33, v35
	s_nop 6
	global_store_dword v[16:17], v6, off nt
	global_store_dword v[16:17], v7, off offset:128 nt
	global_store_dword v[16:17], v8, off offset:256 nt
	v_lshl_add_u64 v[68:69], v[10:11], 0, v[32:33]
	global_store_dword v[68:69], v9, off nt
	ds_read_b128 v[6:9], v81 offset:5536
	s_waitcnt lgkmcnt(0)
	v_mfma_f32_16x16x32_bf16 v[12:15], v[12:15], v[6:9], 0
	v_mov_b32_e32 v37, v35
	v_lshl_add_u64 v[72:73], v[10:11], 0, v[36:37]
	v_mov_b32_e32 v39, v35
	s_nop 4
	global_store_dword v[16:17], v12, off offset:64 nt
	global_store_dword v[72:73], v13, off offset:128 nt
	global_store_dword v[72:73], v14, off offset:256 nt
	global_store_dword v[68:69], v15, off offset:64 nt
	ds_read_b128 v[12:15], v81 offset:8096
	v_mov_b32_e32 v41, v35
	v_mov_b32_e32 v43, v35
	v_mov_b32_e32 v49, v35
	s_waitcnt lgkmcnt(0)
	v_mfma_f32_16x16x32_bf16 v[68:71], v[12:15], v[2:5], 0
	s_nop 7
	global_store_dword v[16:17], v68, off offset:2048 nt
	global_store_dword v[16:17], v69, off offset:2176 nt
	global_store_dword v[16:17], v70, off offset:2304 nt
	v_mfma_f32_16x16x32_bf16 v[12:15], v[12:15], v[6:9], 0
	v_lshl_add_u64 v[16:17], v[10:11], 0, v[38:39]
	global_store_dword v[16:17], v71, off nt
	s_nop 5
	global_store_dword v[72:73], v12, off offset:2048 nt
	global_store_dword v[72:73], v13, off offset:2176 nt
	global_store_dword v[72:73], v14, off offset:2304 nt
	global_store_dword v[16:17], v15, off offset:64 nt
	ds_read_b128 v[12:15], v81 offset:9376
	s_waitcnt lgkmcnt(0)
	v_mfma_f32_16x16x32_bf16 v[68:71], v[12:15], v[2:5], 0
	v_lshl_add_u64 v[16:17], v[10:11], 0, v[40:41]
	v_mov_b32_e32 v45, v35
	v_mov_b32_e32 v51, v35
	v_mfma_f32_16x16x32_bf16 v[12:15], v[12:15], v[6:9], 0
	s_nop 3
	global_store_dword v[16:17], v68, off nt
	v_lshl_add_u64 v[16:17], v[10:11], 0, v[42:43]
	global_store_dword v[16:17], v69, off nt
	v_lshl_add_u64 v[68:69], v[10:11], 0, v[48:49]
	v_lshl_add_u64 v[16:17], v[10:11], 0, v[44:45]
	v_mov_b32_e32 v47, v35
	global_store_dword v[68:69], v12, off nt
	v_lshl_add_u64 v[68:69], v[10:11], 0, v[50:51]
	v_mov_b32_e32 v53, v35
	global_store_dword v[16:17], v70, off nt
	v_lshl_add_u64 v[16:17], v[10:11], 0, v[46:47]
	global_store_dword v[68:69], v13, off nt
	v_lshl_add_u64 v[12:13], v[10:11], 0, v[52:53]
	global_store_dword v[16:17], v71, off nt
	global_store_dword v[12:13], v14, off nt
	global_store_dword v[16:17], v15, off offset:64 nt
	ds_read_b128 v[12:15], v81 offset:10656
	s_waitcnt lgkmcnt(0)
	v_mfma_f32_16x16x32_bf16 v[2:5], v[12:15], v[2:5], 0
	v_mov_b32_e32 v55, v35
	v_lshl_add_u64 v[16:17], v[10:11], 0, v[54:55]
	v_mov_b32_e32 v57, v35
	s_nop 4
	global_store_dword v[16:17], v2, off nt
	v_lshl_add_u64 v[16:17], v[10:11], 0, v[56:57]
	v_mov_b32_e32 v59, v35
	v_mov_b32_e32 v61, v35
	global_store_dword v[16:17], v3, off nt
	v_lshl_add_u64 v[2:3], v[10:11], 0, v[58:59]
	v_lshl_add_u64 v[16:17], v[10:11], 0, v[60:61]
	global_store_dword v[2:3], v4, off nt
	global_store_dword v[16:17], v5, off nt
	v_mfma_f32_16x16x32_bf16 v[2:5], v[12:15], v[6:9], 0
	v_mov_b32_e32 v63, v35
	v_lshl_add_u64 v[6:7], v[10:11], 0, v[62:63]
	v_mov_b32_e32 v65, v35
	v_mov_b32_e32 v67, v35
	s_nop 3
	global_store_dword v[6:7], v2, off nt
	v_lshl_add_u64 v[6:7], v[10:11], 0, v[64:65]
	global_store_dword v[6:7], v3, off nt
	v_lshl_add_u64 v[2:3], v[10:11], 0, v[66:67]
	global_store_dword v[2:3], v4, off nt
	global_store_dword v[16:17], v5, off offset:64 nt
	s_waitcnt lgkmcnt(0)
	s_branch .LBB0_395

.LBB0_492:
	s_lshl_b32 s0, s26, 2
	s_or_b32 s9, s0, s34
	s_lshl_b32 s0, s25, 4
	s_lshl_b32 s1, s9, 1
	s_add_i32 s0, s0, s18
	s_add_i32 s8, s0, s1
	s_lshl_b32 s0, s9, 2
	v_mov_b32_e32 v2, s0
	global_load_dword v2, v2, s[62:63]
	s_mov_b32 s14, 0
	s_mov_b32 s15, 1
	s_mov_b32 s1, s14
	v_and_b32_e32 v7, 64, v203
	v_add_u32_e32 v8, -1, v203
	v_cmp_lt_i32_e32 vcc, v8, v7
	s_lshl_b32 s10, s9, 7
	s_mov_b32 s11, s14
	v_cndmask_b32_e32 v8, v8, v203, vcc
	v_lshlrev_b32_e32 v8, 2, v8
	s_waitcnt vmcnt(0)
	v_mul_f32_e32 v2, 0x3fb8aa3b, v2
	v_exp_f32_e32 v6, v2
	v_add_u32_e32 v2, s3, v76
	v_ashrrev_i32_e32 v3, 31, v2
	v_lshlrev_b64 v[4:5], 6, v[2:3]
	v_lshl_add_u64 v[4:5], s[64:65], 0, v[4:5]
	v_lshl_add_u64 v[4:5], v[4:5], 0, s[0:1]
	global_load_dword v4, v[4:5], off
	v_lshlrev_b64 v[2:3], 11, v[2:3]
	v_lshl_add_u64 v[2:3], s[60:61], 0, v[2:3]
	v_lshl_add_u64 v[14:15], v[2:3], 0, s[10:11]
	s_waitcnt vmcnt(0)
	v_mul_f32_e64 v5, v4, -v6
	ds_bpermute_b32 v8, v8, v5
	s_waitcnt lgkmcnt(0)
	v_fma_f32 v8, v4, -v6, v8
	v_cndmask_b32_e64 v5, v8, v5, s[46:47]
	v_add_u32_e32 v8, -2, v203
	v_cmp_lt_i32_e32 vcc, v8, v7
	s_nop 1
	v_cndmask_b32_e32 v8, v8, v203, vcc
	v_lshlrev_b32_e32 v8, 2, v8
	ds_bpermute_b32 v8, v8, v5
	s_waitcnt lgkmcnt(0)
	v_add_f32_e32 v8, v5, v8
	v_cndmask_b32_e64 v5, v8, v5, s[50:51]
	v_add_u32_e32 v8, -4, v203
	v_cmp_lt_i32_e32 vcc, v8, v7
	s_nop 1
	v_cndmask_b32_e32 v8, v8, v203, vcc
	v_lshlrev_b32_e32 v8, 2, v8
	ds_bpermute_b32 v8, v8, v5
	s_waitcnt lgkmcnt(0)
	v_add_f32_e32 v8, v5, v8
	v_cndmask_b32_e64 v5, v8, v5, s[52:53]
	v_add_u32_e32 v8, -8, v203
	v_cmp_lt_i32_e32 vcc, v8, v7
	s_nop 1
	v_cndmask_b32_e32 v8, v8, v203, vcc
	v_lshlrev_b32_e32 v8, 2, v8
	ds_bpermute_b32 v8, v8, v5
	s_waitcnt lgkmcnt(0)
	v_add_f32_e32 v8, v5, v8
	v_cndmask_b32_e64 v5, v8, v5, s[54:55]
	v_add_u32_e32 v8, -16, v203
	v_cmp_lt_i32_e32 vcc, v8, v7
	s_nop 1
	v_cndmask_b32_e32 v8, v8, v203, vcc
	v_lshlrev_b32_e32 v8, 2, v8
	ds_bpermute_b32 v8, v8, v5
	s_waitcnt lgkmcnt(0)
	v_add_f32_e32 v8, v5, v8
	v_cndmask_b32_e64 v5, v8, v5, s[56:57]
	v_subrev_u32_e32 v8, 32, v203
	v_cmp_lt_i32_e32 vcc, v8, v7
	s_nop 1
	v_cndmask_b32_e32 v7, v8, v203, vcc
	v_lshlrev_b32_e32 v7, 2, v7
	ds_bpermute_b32 v7, v7, v5
	s_waitcnt lgkmcnt(0)
	v_add_f32_e32 v7, v5, v7
	v_cndmask_b32_e64 v5, v7, v5, s[42:43]
	v_lshl_or_b32 v7, v203, 2, v251
	ds_bpermute_b32 v27, v7, v5
	s_waitcnt lgkmcnt(0)
	v_sub_f32_e32 v7, v27, v5
	v_fmac_f32_e32 v5, v4, v6
	v_cndmask_b32_e64 v5, v5, v7, s[38:39]
	v_mul_f32_e32 v5, 0x3fb8aa3b, v5
	v_exp_f32_e32 v5, v5
	s_nop 0
	v_mul_f32_e32 v29, v4, v5
	global_load_dwordx4 v[2:5], v[14:15], off offset:48
	global_load_dwordx4 v[6:9], v[14:15], off offset:32
	global_load_dwordx4 v[10:13], v[14:15], off offset:16
	global_load_dwordx4 v[68:71], v[14:15], off
	s_waitcnt vmcnt(0)
	v_lshlrev_b32_e32 v16, 16, v68
	v_mul_f32_e32 v16, v29, v16
	v_and_b32_e32 v17, 0xffff0000, v68
	v_cvt_pk_bf16_f32 v16, v16, s0
	ds_write_b16 v82, v16 offset:18432
	v_mul_f32_e32 v16, v29, v17
	v_lshlrev_b32_e32 v31, 16, v69
	v_cvt_pk_bf16_f32 v16, v16, s0
	ds_write_b16 v82, v16 offset:18576
	v_mul_f32_e32 v16, v29, v31
	v_and_b32_e32 v33, 0xffff0000, v69
	v_cvt_pk_bf16_f32 v16, v16, s0
	ds_write_b16 v82, v16 offset:18720
	v_mul_f32_e32 v16, v29, v33
	v_cvt_pk_bf16_f32 v16, v16, s0
	ds_write_b16 v82, v16 offset:18864
	v_lshlrev_b32_e32 v16, 16, v70
	v_mul_f32_e32 v16, v29, v16
	v_and_b32_e32 v17, 0xffff0000, v70
	v_cvt_pk_bf16_f32 v16, v16, s0
	ds_write_b16 v82, v16 offset:19008
	v_mul_f32_e32 v16, v29, v17
	v_lshlrev_b32_e32 v31, 16, v71
	v_cvt_pk_bf16_f32 v16, v16, s0
	ds_write_b16 v82, v16 offset:19152
	v_mul_f32_e32 v16, v29, v31
	v_and_b32_e32 v33, 0xffff0000, v71
	v_cvt_pk_bf16_f32 v16, v16, s0
	ds_write_b16 v82, v16 offset:19296
	v_mul_f32_e32 v16, v29, v33
	v_cvt_pk_bf16_f32 v16, v16, s0
	ds_write_b16 v82, v16 offset:19440
	v_lshlrev_b32_e32 v16, 16, v10
	v_and_b32_e32 v10, 0xffff0000, v10
	v_mul_f32_e32 v10, v29, v10
	v_lshlrev_b32_e32 v17, 16, v11
	v_cvt_pk_bf16_f32 v10, v10, s0
	ds_write_b16 v82, v10 offset:19728
	v_mul_f32_e32 v10, v29, v17
	v_and_b32_e32 v11, 0xffff0000, v11
	v_cvt_pk_bf16_f32 v10, v10, s0
	ds_write_b16 v82, v10 offset:19872
	v_mul_f32_e32 v10, v29, v11
	v_cvt_pk_bf16_f32 v10, v10, s0
	ds_write_b16 v82, v10 offset:20016
	v_lshlrev_b32_e32 v10, 16, v12
	v_mul_f32_e32 v10, v29, v10
	v_and_b32_e32 v11, 0xffff0000, v12
	v_cvt_pk_bf16_f32 v10, v10, s0
	ds_write_b16 v82, v10 offset:20160
	v_mul_f32_e32 v10, v29, v11
	v_lshlrev_b32_e32 v12, 16, v13
	v_cvt_pk_bf16_f32 v10, v10, s0
	ds_write_b16 v82, v10 offset:20304
	v_mul_f32_e32 v10, v29, v12
	v_and_b32_e32 v13, 0xffff0000, v13
	v_cvt_pk_bf16_f32 v10, v10, s0
	ds_write_b16 v82, v10 offset:20448
	v_mul_f32_e32 v10, v29, v13
	v_cvt_pk_bf16_f32 v10, v10, s0
	ds_write_b16 v82, v10 offset:20592
	v_lshlrev_b32_e32 v10, 16, v6
	v_and_b32_e32 v6, 0xffff0000, v6
	v_mul_f32_e32 v6, v29, v6
	v_lshlrev_b32_e32 v11, 16, v7
	v_cvt_pk_bf16_f32 v6, v6, s0
	ds_write_b16 v82, v6 offset:20880
	v_mul_f32_e32 v6, v29, v11
	v_and_b32_e32 v7, 0xffff0000, v7
	v_cvt_pk_bf16_f32 v6, v6, s0
	ds_write_b16 v82, v6 offset:21024
	v_mul_f32_e32 v6, v29, v7
	v_cvt_pk_bf16_f32 v6, v6, s0
	ds_write_b16 v82, v6 offset:21168
	v_lshlrev_b32_e32 v6, 16, v8
	v_mul_f32_e32 v6, v29, v6
	v_and_b32_e32 v7, 0xffff0000, v8
	v_cvt_pk_bf16_f32 v6, v6, s0
	ds_write_b16 v82, v6 offset:21312
	v_mul_f32_e32 v6, v29, v7
	v_lshlrev_b32_e32 v8, 16, v9
	v_cvt_pk_bf16_f32 v6, v6, s0
	ds_write_b16 v82, v6 offset:21456
	v_mul_f32_e32 v6, v29, v8
	v_and_b32_e32 v9, 0xffff0000, v9
	v_cvt_pk_bf16_f32 v6, v6, s0
	ds_write_b16 v82, v6 offset:21600
	v_mul_f32_e32 v6, v29, v9
	v_cvt_pk_bf16_f32 v6, v6, s0
	ds_write_b16 v82, v6 offset:21744
	v_lshlrev_b32_e32 v6, 16, v2
	v_and_b32_e32 v2, 0xffff0000, v2
	v_mul_f32_e32 v2, v29, v2
	v_lshlrev_b32_e32 v7, 16, v3
	v_cvt_pk_bf16_f32 v2, v2, s0
	ds_write_b16 v82, v2 offset:22032
	v_mul_f32_e32 v2, v29, v7
	v_and_b32_e32 v3, 0xffff0000, v3
	v_cvt_pk_bf16_f32 v2, v2, s0
	ds_write_b16 v82, v2 offset:22176
	v_mul_f32_e32 v2, v29, v3
	v_cvt_pk_bf16_f32 v2, v2, s0
	ds_write_b16 v82, v2 offset:22320
	v_lshlrev_b32_e32 v2, 16, v4
	v_mul_f32_e32 v2, v29, v2
	v_and_b32_e32 v3, 0xffff0000, v4
	v_cvt_pk_bf16_f32 v2, v2, s0
	ds_write_b16 v82, v2 offset:22464
	v_mul_f32_e32 v2, v29, v3
	v_lshlrev_b32_e32 v4, 16, v5
	v_cvt_pk_bf16_f32 v2, v2, s0
	ds_write_b16 v82, v2 offset:22608
	v_mul_f32_e32 v2, v29, v4
	v_and_b32_e32 v5, 0xffff0000, v5
	v_cvt_pk_bf16_f32 v2, v2, s0
	v_mul_f32_e32 v16, v29, v16
	v_mul_f32_e32 v10, v29, v10
	v_mul_f32_e32 v6, v29, v6
	ds_write_b16 v82, v2 offset:22752
	v_mul_f32_e32 v2, v29, v5
	v_cvt_pk_bf16_f32 v16, v16, s0
	v_cvt_pk_bf16_f32 v10, v10, s0
	v_cvt_pk_bf16_f32 v6, v6, s0
	v_cvt_pk_bf16_f32 v2, v2, s0
	ds_write_b16 v82, v16 offset:19584
	ds_write_b16 v82, v10 offset:20736
	ds_write_b16 v82, v6 offset:21888
	ds_write_b16 v82, v2 offset:22896
	global_load_dwordx4 v[2:5], v[14:15], off offset:112
	global_load_dwordx4 v[6:9], v[14:15], off offset:96
	global_load_dwordx4 v[10:13], v[14:15], off offset:80
	s_nop 0
	global_load_dwordx4 v[14:17], v[14:15], off offset:64
	s_waitcnt vmcnt(0)
	v_lshlrev_b32_e32 v31, 16, v14
	v_and_b32_e32 v14, 0xffff0000, v14
	v_mul_f32_e32 v14, v29, v14
	v_lshlrev_b32_e32 v33, 16, v15
	v_cvt_pk_bf16_f32 v14, v14, s0
	ds_write_b16 v82, v14 offset:23184
	v_mul_f32_e32 v14, v29, v33
	v_and_b32_e32 v15, 0xffff0000, v15
	v_cvt_pk_bf16_f32 v14, v14, s0
	ds_write_b16 v82, v14 offset:23328
	v_mul_f32_e32 v14, v29, v15
	v_cvt_pk_bf16_f32 v14, v14, s0
	ds_write_b16 v82, v14 offset:23472
	v_lshlrev_b32_e32 v14, 16, v16
	v_mul_f32_e32 v14, v29, v14
	v_and_b32_e32 v15, 0xffff0000, v16
	v_cvt_pk_bf16_f32 v14, v14, s0
	ds_write_b16 v82, v14 offset:23616
	v_mul_f32_e32 v14, v29, v15
	v_lshlrev_b32_e32 v16, 16, v17
	v_cvt_pk_bf16_f32 v14, v14, s0
	ds_write_b16 v82, v14 offset:23760
	v_mul_f32_e32 v14, v29, v16
	v_and_b32_e32 v17, 0xffff0000, v17
	v_cvt_pk_bf16_f32 v14, v14, s0
	ds_write_b16 v82, v14 offset:23904
	v_mul_f32_e32 v14, v29, v17
	v_cvt_pk_bf16_f32 v14, v14, s0
	ds_write_b16 v82, v14 offset:24048
	v_lshlrev_b32_e32 v14, 16, v10
	v_and_b32_e32 v10, 0xffff0000, v10
	v_mul_f32_e32 v10, v29, v10
	v_lshlrev_b32_e32 v15, 16, v11
	v_cvt_pk_bf16_f32 v10, v10, s0
	ds_write_b16 v82, v10 offset:24336
	v_mul_f32_e32 v10, v29, v15
	v_and_b32_e32 v11, 0xffff0000, v11
	v_cvt_pk_bf16_f32 v10, v10, s0
	ds_write_b16 v82, v10 offset:24480
	v_mul_f32_e32 v10, v29, v11
	v_cvt_pk_bf16_f32 v10, v10, s0
	ds_write_b16 v82, v10 offset:24624
	v_lshlrev_b32_e32 v10, 16, v12
	v_mul_f32_e32 v10, v29, v10
	v_and_b32_e32 v11, 0xffff0000, v12
	v_cvt_pk_bf16_f32 v10, v10, s0
	ds_write_b16 v82, v10 offset:24768
	v_mul_f32_e32 v10, v29, v11
	v_lshlrev_b32_e32 v12, 16, v13
	v_cvt_pk_bf16_f32 v10, v10, s0
	ds_write_b16 v82, v10 offset:24912
	v_mul_f32_e32 v10, v29, v12
	v_and_b32_e32 v13, 0xffff0000, v13
	v_cvt_pk_bf16_f32 v10, v10, s0
	ds_write_b16 v82, v10 offset:25056
	v_mul_f32_e32 v10, v29, v13
	v_cvt_pk_bf16_f32 v10, v10, s0
	ds_write_b16 v82, v10 offset:25200
	v_lshlrev_b32_e32 v10, 16, v6
	v_and_b32_e32 v6, 0xffff0000, v6
	v_mul_f32_e32 v6, v29, v6
	v_lshlrev_b32_e32 v11, 16, v7
	v_cvt_pk_bf16_f32 v6, v6, s0
	ds_write_b16 v82, v6 offset:25488
	v_mul_f32_e32 v6, v29, v11
	v_and_b32_e32 v7, 0xffff0000, v7
	v_cvt_pk_bf16_f32 v6, v6, s0
	ds_write_b16 v82, v6 offset:25632
	v_mul_f32_e32 v6, v29, v7
	v_cvt_pk_bf16_f32 v6, v6, s0
	ds_write_b16 v82, v6 offset:25776
	v_lshlrev_b32_e32 v6, 16, v8
	v_mul_f32_e32 v6, v29, v6
	v_and_b32_e32 v7, 0xffff0000, v8
	v_cvt_pk_bf16_f32 v6, v6, s0
	ds_write_b16 v82, v6 offset:25920
	v_mul_f32_e32 v6, v29, v7
	v_lshlrev_b32_e32 v8, 16, v9
	v_cvt_pk_bf16_f32 v6, v6, s0
	ds_write_b16 v82, v6 offset:26064
	v_mul_f32_e32 v6, v29, v8
	v_and_b32_e32 v9, 0xffff0000, v9
	v_cvt_pk_bf16_f32 v6, v6, s0
	ds_write_b16 v82, v6 offset:26208
	v_mul_f32_e32 v6, v29, v9
	v_cvt_pk_bf16_f32 v6, v6, s0
	ds_write_b16 v82, v6 offset:26352
	v_lshlrev_b32_e32 v6, 16, v2
	v_and_b32_e32 v2, 0xffff0000, v2
	v_mul_f32_e32 v2, v29, v2
	v_lshlrev_b32_e32 v7, 16, v3
	v_cvt_pk_bf16_f32 v2, v2, s0
	ds_write_b16 v82, v2 offset:26640
	v_mul_f32_e32 v2, v29, v7
	v_and_b32_e32 v3, 0xffff0000, v3
	v_cvt_pk_bf16_f32 v2, v2, s0
	ds_write_b16 v82, v2 offset:26784
	v_mul_f32_e32 v2, v29, v3
	v_cvt_pk_bf16_f32 v2, v2, s0
	ds_write_b16 v82, v2 offset:26928
	v_lshlrev_b32_e32 v2, 16, v4
	v_mul_f32_e32 v2, v29, v2
	v_and_b32_e32 v3, 0xffff0000, v4
	v_cvt_pk_bf16_f32 v2, v2, s0
	ds_write_b16 v82, v2 offset:27072
	v_mul_f32_e32 v2, v29, v3
	v_lshlrev_b32_e32 v4, 16, v5
	v_cvt_pk_bf16_f32 v2, v2, s0
	ds_write_b16 v82, v2 offset:27216
	v_mul_f32_e32 v2, v29, v4
	v_and_b32_e32 v5, 0xffff0000, v5
	v_cvt_pk_bf16_f32 v2, v2, s0
	v_mul_f32_e32 v31, v29, v31
	v_mul_f32_e32 v14, v29, v14
	v_mul_f32_e32 v10, v29, v10
	v_mul_f32_e32 v6, v29, v6
	ds_write_b16 v82, v2 offset:27360
	v_mul_f32_e32 v2, v29, v5
	v_cvt_pk_bf16_f32 v31, v31, s0
	v_cvt_pk_bf16_f32 v14, v14, s0
	v_cvt_pk_bf16_f32 v10, v10, s0
	v_cvt_pk_bf16_f32 v6, v6, s0
	v_cvt_pk_bf16_f32 v2, v2, s0
	ds_write_b16 v82, v31 offset:23040
	ds_write_b16 v82, v14 offset:24192
	ds_write_b16 v82, v10 offset:25344
	ds_write_b16 v82, v6 offset:26496
	ds_write_b16 v82, v2 offset:27504
	s_and_saveexec_b64 s[0:1], s[48:49]
	s_xor_b64 s[0:1], exec, s[0:1]
	s_ashr_i32 s9, s8, 31
	s_ashr_i32 s3, s2, 31
	s_or_saveexec_b64 s[0:1], s[0:1]
	v_mov_b64_e32 v[4:5], s[2:3]
	v_mov_b64_e32 v[2:3], s[8:9]
	s_xor_b64 exec, exec, s[0:1]
	s_cbranch_execz .LBB0_496
	v_mul_f32_e32 v2, 0x3fb8aa3b, v27
	s_ashr_i32 s9, s8, 31
	s_ashr_i32 s3, s2, 31
	s_mul_i32 s11, s8, 0x110
	v_exp_f32_e32 v2, v2
	s_mul_hi_i32 s10, s8, 0x110
	s_add_u32 s14, s22, s11
	s_addc_u32 s15, s23, s10
	s_lshl_b64 s[10:11], s[2:3], 2
	s_add_u32 s10, s14, s10
	s_addc_u32 s11, s15, s11
	global_store_dword v35, v2, s[10:11] nt
	v_mov_b64_e32 v[4:5], s[2:3]
	v_mov_b64_e32 v[2:3], s[8:9]

.LBB0_498:
	v_add_u32_e32 v27, s1, v84
	ds_read_b128 v[14:17], v27
	ds_read_b128 v[68:71], v27 offset:64
	s_addk_i32 s1, 0x1200
	s_cmpk_eq_i32 s1, 0x4800
	s_waitcnt lgkmcnt(1)
	v_mfma_f32_16x16x32_bf16 v[14:17], v[2:5], v[14:17], 0
	s_waitcnt lgkmcnt(0)
	v_mfma_f32_16x16x32_bf16 v[14:17], v[6:9], v[68:71], v[14:17]
	ds_read_b128 v[68:71], v27 offset:2368
	s_nop 6
	v_cvt_pk_bf16_f32 v14, v14, s0
	global_store_short v[12:13], v14, off offset:-512 nt
	v_cvt_pk_bf16_f32 v14, v15, s0
	global_store_short v[12:13], v14, off offset:-256 nt
	v_cvt_pk_bf16_f32 v14, v16, s0
	global_store_short v[12:13], v14, off nt
	v_cvt_pk_bf16_f32 v14, v17, s0
	global_store_short v[12:13], v14, off offset:256 nt
	ds_read_b128 v[14:17], v27 offset:2304
	s_waitcnt lgkmcnt(0)
	v_mfma_f32_16x16x32_bf16 v[14:17], v[2:5], v[14:17], 0
	v_mfma_f32_16x16x32_bf16 v[14:17], v[6:9], v[68:71], v[14:17]
	s_nop 7
	v_cvt_pk_bf16_f32 v14, v14, s0
	global_store_short v[12:13], v14, off offset:-480 nt
	v_cvt_pk_bf16_f32 v14, v15, s0
	global_store_short v[12:13], v14, off offset:-224 nt
	v_cvt_pk_bf16_f32 v14, v16, s0
	global_store_short v[12:13], v14, off offset:32 nt
	v_cvt_pk_bf16_f32 v14, v17, s0
	global_store_short v[12:13], v14, off offset:288 nt
	v_lshl_add_u64 v[12:13], v[12:13], 0, 64
	s_cbranch_scc0 .LBB0_498
	s_add_i32 s0, s0, 1
	s_cmp_eq_u32 s0, 4
	v_lshl_add_u64 v[10:11], v[10:11], 0, s[28:29]
	s_cbranch_scc0 .LBB0_497
	s_waitcnt lgkmcnt(0)
	s_barrier
	s_branch .LBB0_395
